# v28: v26 + late gate load of the attention-combine pass hoisted + router-logit weight reads from LDS double-buffered (next ds_read issued before the FMAs of the current one)
# speedup vs baseline: 1.0010x; 1.0010x over previous
; __device__ __forceinline__ float rdl(float v, int l) { return __builtin_bit_cast(float, __builtin_amdgcn_readlane(__builtin_bit_cast(int, v), l)); }
; __device__ __forceinline__ void ph6_hf(const Frame& F, const Args& A) {
;     ...
;     for (int g = gw; g < S_; g += NGW) {
;         const int h = g & 7, row0 = (g >> 3) * 8, blk = h * 32 + (row0 >> 8), rr0 = row0 & 255;
;         const int np = __builtin_amdgcn_readfirstlane(NPART[blk]);
;         const float* pm = PML + (size_t)blk * MAXP * 512 + rr0 + mlo; const bf16* po = PO + (size_t)blk * MAXP * 32768 + (size_t)rr0 * 128 + 2 * lane;
;         unsigned gz[8], ov[8]; float M[8], L[8]; f32x2_t a[8];
;         { const float ml = pm[0];
; #pragma unroll
;           for (int q = 0; q < 8; ++q) { ov[q] = *(const unsigned*)(po + q * 128); gz[q] = *(const unsigned short*)(A.ws + WS_Z8 + (size_t)(row0 + q) * pg8::Z8LD + 1024 + h * 128 + 2 * lane); }
; #pragma unroll
;           for (int q = 0; q < 8; ++q) { M[q] = rdl(ml, q); L[q] = rdl(ml, 8 + q); a[q].x = bflo(ov[q]); a[q].y = bfhi(ov[q]); } }
; #pragma unroll 1
;         for (int p = 1; p < np; ++p) { const float ml = pm[(size_t)p * 512];
.LBB0_972:
	s_ashr_i32 s20, s26, 8
	s_add_i32 s4, s20, s35
	s_ashr_i32 s5, s4, 31
	s_and_b32 s14, s26, -8
	s_and_b32 s10, s26, 0xf8
	s_lshl_b64 s[6:7], s[4:5], 2
	s_add_u32 s6, s31, s6
	s_addc_u32 s7, s33, s7
	global_load_dword v22, v35, s[6:7]
	s_lshl_b64 s[6:7], s[4:5], 15
	s_add_u32 s6, s29, s6
	s_addc_u32 s7, s30, s7
	s_lshl_b32 s8, s10, 2
	s_add_u32 s8, s6, s8
	s_addc_u32 s9, s7, 0
	s_lshl_b64 s[4:5], s[4:5], 20
	s_add_u32 s4, s27, s4
	s_addc_u32 s5, s28, s5
	s_lshl_b32 s6, s10, 8
	s_add_u32 s6, s4, s6
	s_addc_u32 s7, s5, 0
	s_mul_i32 s5, s14, 0x1800
	s_mul_hi_i32 s4, s14, 0x1800
	s_add_u32 s5, s88, s5
	global_load_dword v23, v1, s[8:9]
	global_load_dword v24, v42, s[6:7]
	s_addc_u32 s8, s89, s4
	s_add_u32 s4, s5, s36
	s_addc_u32 s5, s8, 0
	s_or_b32 s18, s14, 1
	v_lshl_add_u64 v[8:9], s[4:5], 0, v[34:35]
	s_mul_i32 s5, s18, 0x1800
	s_mul_hi_i32 s4, s18, 0x1800
	s_add_u32 s5, s88, s5
	s_addc_u32 s8, s89, s4
	s_add_u32 s4, s5, s36
	s_addc_u32 s5, s8, 0
	s_or_b32 s16, s14, 2
	v_lshl_add_u64 v[10:11], s[4:5], 0, v[34:35]
	s_mul_i32 s5, s16, 0x1800
	s_mul_hi_i32 s4, s16, 0x1800
	s_add_u32 s5, s88, s5
	s_addc_u32 s8, s89, s4
	s_add_u32 s4, s5, s36
	s_addc_u32 s5, s8, 0
	s_or_b32 s12, s14, 3
	v_lshl_add_u64 v[12:13], s[4:5], 0, v[34:35]
	s_mul_i32 s5, s12, 0x1800
	s_mul_hi_i32 s4, s12, 0x1800
	s_add_u32 s5, s88, s5
	s_addc_u32 s8, s89, s4
	s_add_u32 s4, s5, s36
	s_addc_u32 s5, s8, 0
	s_or_b32 s10, s14, 4
	v_lshl_add_u64 v[14:15], s[4:5], 0, v[34:35]
	s_mul_i32 s5, s10, 0x1800
	s_mul_hi_i32 s4, s10, 0x1800
	s_add_u32 s5, s88, s5
	s_addc_u32 s8, s89, s4
	s_add_u32 s4, s5, s36
	s_addc_u32 s5, s8, 0
	s_or_b32 s8, s14, 5
	v_add_co_u32_e32 v8, vcc, s37, v8
	v_lshl_add_u64 v[16:17], s[4:5], 0, v[34:35]
	s_mul_i32 s5, s8, 0x1800
	v_addc_co_u32_e32 v9, vcc, 0, v9, vcc
	s_mul_hi_i32 s4, s8, 0x1800
	s_add_u32 s5, s88, s5
	v_add_co_u32_e32 v10, vcc, s37, v10
	s_addc_u32 s9, s89, s4
	s_nop 0
	v_addc_co_u32_e32 v11, vcc, 0, v11, vcc
	s_add_u32 s4, s5, s36
	v_add_co_u32_e32 v12, vcc, s37, v12
	s_addc_u32 s5, s9, 0
	s_nop 0
	v_addc_co_u32_e32 v13, vcc, 0, v13, vcc
	v_lshl_add_u64 v[18:19], s[4:5], 0, v[34:35]
	s_or_b32 s4, s14, 6
	v_add_co_u32_e32 v14, vcc, s37, v14
	s_mul_i32 s9, s4, 0x1800
	s_nop 0
	v_addc_co_u32_e32 v15, vcc, 0, v15, vcc
	s_mul_hi_i32 s5, s4, 0x1800
	s_add_u32 s9, s88, s9
	v_add_co_u32_e32 v16, vcc, s37, v16
	s_addc_u32 s5, s89, s5
	s_nop 0
	v_addc_co_u32_e32 v17, vcc, 0, v17, vcc
	s_add_u32 s22, s9, s36
	v_add_co_u32_e32 v18, vcc, s37, v18
	s_addc_u32 s23, s5, 0
	s_nop 0
	v_addc_co_u32_e32 v19, vcc, 0, v19, vcc
	v_lshl_add_u64 v[20:21], s[22:23], 0, v[34:35]
	v_add_co_u32_e32 v20, vcc, s37, v20
	global_load_dword v25, v42, s[6:7] offset:256
	global_load_dword v27, v42, s[6:7] offset:512
	global_load_dword v30, v42, s[6:7] offset:768
	global_load_dword v31, v42, s[6:7] offset:1024
	global_load_dword v36, v42, s[6:7] offset:1280
	global_load_dword v37, v42, s[6:7] offset:1536
	v_addc_co_u32_e32 v21, vcc, 0, v21, vcc
	global_load_ushort v48, v[8:9], off offset:1024
	global_load_ushort v49, v[10:11], off offset:1024
	global_load_ushort v50, v[12:13], off offset:1024
	global_load_ushort v44, v[14:15], off offset:1024
	global_load_ushort v45, v[16:17], off offset:1024
	global_load_ushort v46, v[18:19], off offset:1024
	global_load_ushort v43, v[20:21], off offset:1024
	global_load_dword v10, v42, s[6:7] offset:1792
	s_or_b32 s6, s26, 7
	s_mul_i32 s7, s6, 0x1800
	s_mul_hi_i32 s5, s6, 0x1800
	s_add_u32 s7, s88, s7
	s_addc_u32 s5, s89, s5
	s_add_u32 s22, s7, s36
	s_addc_u32 s23, s5, 0
	v_lshl_add_u64 v[8:9], s[22:23], 0, v[34:35]
	v_add_co_u32_e32 v8, vcc, s37, v8
	s_nop 1
	v_addc_co_u32_e32 v9, vcc, 0, v9, vcc
	global_load_ushort v47, v[8:9], off offset:1024
	s_waitcnt vmcnt(0)
	v_readfirstlane_b32 s5, v22
	v_readlane_b32 s7, v23, 0
	v_readlane_b32 s11, v23, 8
	v_lshlrev_b32_e32 v32, 16, v24
	v_and_b32_e32 v33, 0xffff0000, v24
	v_readlane_b32 s9, v23, 1
	v_readlane_b32 s15, v23, 9
	v_readlane_b32 s13, v23, 2
	v_readlane_b32 s19, v23, 10
	v_readlane_b32 s17, v23, 3
	v_readlane_b32 s23, v23, 11
	v_readlane_b32 s22, v23, 4
	v_readlane_b32 s25, v23, 12
	v_readlane_b32 s24, v23, 5
	v_readlane_b32 s39, v23, 13
	v_readlane_b32 s38, v23, 6
	v_readlane_b32 s41, v23, 14
	v_readlane_b32 s40, v23, 7
	v_readlane_b32 s42, v23, 15
	s_cmp_lt_i32 s5, 2
	v_lshlrev_b32_e32 v28, 16, v25
	v_and_b32_e32 v29, 0xffff0000, v25
	v_lshlrev_b32_e32 v26, 16, v27
	v_and_b32_e32 v27, 0xffff0000, v27
	v_lshlrev_b32_e32 v24, 16, v30
	v_and_b32_e32 v25, 0xffff0000, v30
	v_lshlrev_b32_e32 v18, 16, v31
	v_and_b32_e32 v19, 0xffff0000, v31
	v_lshlrev_b32_e32 v16, 16, v36
	v_and_b32_e32 v17, 0xffff0000, v36
	v_lshlrev_b32_e32 v12, 16, v37
	v_and_b32_e32 v13, 0xffff0000, v37
	v_lshlrev_b32_e32 v8, 16, v10
	v_and_b32_e32 v10, 0xffff0000, v10
	s_cbranch_scc1 .LBB0_970
	s_lshl_b32 s21, s26, 2
	s_and_b32 s43, s21, 0x3e0
	s_lshl_b32 s21, s26, 8
	s_and_b32 s46, s21, 0xf800
	s_ashr_i32 s21, s20, 31
	s_lshl_b64 s[44:45], s[20:21], 15
	s_lshl_b64 s[20:21], s[20:21], 20
	s_or_b32 s44, s44, s43
	s_or_b32 s20, s20, s46
	s_add_i32 s5, s5, -1
	v_lshl_add_u64 v[38:39], v[4:5], 0, s[44:45]
	v_lshl_add_u64 v[40:41], v[6:7], 0, s[20:21]
	v_mov_b32_e32 v14, s42
	v_mov_b32_e32 v20, s41
	v_mov_b32_e32 v23, s39
	v_mov_b32_e32 v22, s25
	v_mov_b32_e32 v31, s23
	v_mov_b32_e32 v30, s19
	v_mov_b32_e32 v37, s15
	v_mov_b32_e32 v36, s11
	v_mov_b32_e32 v51, s40
	v_mov_b32_e32 v52, s38
	v_mov_b32_e32 v53, s24
	v_mov_b32_e32 v54, s22
	v_mov_b32_e32 v55, s17
	v_mov_b32_e32 v56, s13
	v_mov_b32_e32 v57, s9
	v_mov_b32_e32 v58, s7

; __device__ __forceinline__ void ph9_router(const Frame& F, const Args& A) {
;     ...
;             for (int g = 0; g < 4; ++g) { float q[4][4];
; #pragma unroll
;                 for (int el = 0; el < 4; ++el) { f32x4 a0 = {0.f, 0.f, 0.f, 0.f}, a1 = a0, a2 = a0, a3 = a0;
; #pragma unroll
;                     for (int j = 0; j < 8; ++j) { const f32x4 w = wl[(4 * g + el) * 512 + lane + 64 * j];
;                         a0 += hv[0][j] * w; a1 += hv[1][j] * w; a2 += hv[2][j] * w; a3 += hv[3][j] * w; }
;                     q[0][el] = (a0.x + a0.y) + (a0.z + a0.w); q[1][el] = (a1.x + a1.y) + (a1.z + a1.w); q[2][el] = (a2.x + a2.y) + (a2.z + a2.w); q[3][el] = (a3.x + a3.y) + (a3.z + a3.w); }
.LBB0_1199:
	v_add_u32_e32 v2, s14, v157
	ds_read_b128 v[230:233], v2
	v_cmp_eq_u32_e32 vcc, s14, v158
	s_add_i32 s14, s14, 0x8000
	s_cmp_eq_u32 s14, 0x20000
	ds_read_b128 v[4:7], v2 offset:1024
	s_waitcnt lgkmcnt(1)
	v_pk_fma_f32 v[8:9], v[26:27], v[232:233], 0 op_sel_hi:[1,1,0]
	v_pk_fma_f32 v[144:145], v[30:31], v[230:231], 0 op_sel_hi:[1,1,0]
	v_pk_fma_f32 v[146:147], v[20:21], v[232:233], 0 op_sel_hi:[1,1,0]
	v_pk_fma_f32 v[148:149], v[24:25], v[230:231], 0 op_sel_hi:[1,1,0]
	v_pk_fma_f32 v[150:151], v[14:15], v[232:233], 0 op_sel_hi:[1,1,0]
	v_pk_fma_f32 v[152:153], v[16:17], v[230:231], 0 op_sel_hi:[1,1,0]
	v_pk_fma_f32 v[154:155], v[10:11], v[232:233], 0 op_sel_hi:[1,1,0]
	v_pk_fma_f32 v[160:161], v[12:13], v[230:231], 0 op_sel_hi:[1,1,0]
	ds_read_b128 v[230:233], v2 offset:2048
	s_waitcnt lgkmcnt(1)
	v_pk_fma_f32 v[8:9], v[48:49], v[6:7], v[8:9]
	v_pk_fma_f32 v[144:145], v[52:53], v[4:5], v[144:145]
	v_pk_fma_f32 v[146:147], v[38:39], v[6:7], v[146:147]
	v_pk_fma_f32 v[148:149], v[40:41], v[4:5], v[148:149]
	v_pk_fma_f32 v[150:151], v[28:29], v[6:7], v[150:151]
	v_pk_fma_f32 v[152:153], v[32:33], v[4:5], v[152:153]
	v_pk_fma_f32 v[154:155], v[18:19], v[6:7], v[154:155]
	v_pk_fma_f32 v[160:161], v[22:23], v[4:5], v[160:161]
	ds_read_b128 v[4:7], v2 offset:3072
	s_waitcnt lgkmcnt(1)
	v_pk_fma_f32 v[8:9], v[62:63], v[232:233], v[8:9]
	v_pk_fma_f32 v[144:145], v[64:65], v[230:231], v[144:145]
	v_pk_fma_f32 v[146:147], v[54:55], v[232:233], v[146:147]
	v_pk_fma_f32 v[148:149], v[56:57], v[230:231], v[148:149]
	v_pk_fma_f32 v[150:151], v[42:43], v[232:233], v[150:151]
	v_pk_fma_f32 v[152:153], v[44:45], v[230:231], v[152:153]
	v_pk_fma_f32 v[154:155], v[34:35], v[232:233], v[154:155]
	v_pk_fma_f32 v[160:161], v[36:37], v[230:231], v[160:161]
	ds_read_b128 v[230:233], v2 offset:4096
	s_waitcnt lgkmcnt(1)
	v_pk_fma_f32 v[8:9], v[76:77], v[6:7], v[8:9]
	v_pk_fma_f32 v[144:145], v[80:81], v[4:5], v[144:145]
	v_pk_fma_f32 v[146:147], v[68:69], v[6:7], v[146:147]
	v_pk_fma_f32 v[148:149], v[72:73], v[4:5], v[148:149]
	v_pk_fma_f32 v[150:151], v[58:59], v[6:7], v[150:151]
	v_pk_fma_f32 v[152:153], v[60:61], v[4:5], v[152:153]
	v_pk_fma_f32 v[154:155], v[46:47], v[6:7], v[154:155]
	v_pk_fma_f32 v[160:161], v[50:51], v[4:5], v[160:161]
	ds_read_b128 v[4:7], v2 offset:5120
	s_waitcnt lgkmcnt(1)
	v_pk_fma_f32 v[8:9], v[96:97], v[232:233], v[8:9]
	v_pk_fma_f32 v[144:145], v[100:101], v[230:231], v[144:145]
	v_pk_fma_f32 v[146:147], v[86:87], v[232:233], v[146:147]
	v_pk_fma_f32 v[148:149], v[88:89], v[230:231], v[148:149]
	v_pk_fma_f32 v[150:151], v[74:75], v[232:233], v[150:151]
	v_pk_fma_f32 v[152:153], v[78:79], v[230:231], v[152:153]
	v_pk_fma_f32 v[154:155], v[66:67], v[232:233], v[154:155]
	v_pk_fma_f32 v[160:161], v[70:71], v[230:231], v[160:161]
	ds_read_b128 v[230:233], v2 offset:6144
	s_waitcnt lgkmcnt(1)
	v_pk_fma_f32 v[8:9], v[112:113], v[6:7], v[8:9]
	v_pk_fma_f32 v[144:145], v[116:117], v[4:5], v[144:145]
	v_pk_fma_f32 v[146:147], v[102:103], v[6:7], v[146:147]
	v_pk_fma_f32 v[148:149], v[104:105], v[4:5], v[148:149]
	v_pk_fma_f32 v[150:151], v[90:91], v[6:7], v[150:151]
	v_pk_fma_f32 v[152:153], v[92:93], v[4:5], v[152:153]
	v_pk_fma_f32 v[154:155], v[82:83], v[6:7], v[154:155]
	v_pk_fma_f32 v[160:161], v[84:85], v[4:5], v[160:161]
	ds_read_b128 v[4:7], v2 offset:7168
	s_waitcnt lgkmcnt(1)
	v_pk_fma_f32 v[8:9], v[126:127], v[232:233], v[8:9]
	v_pk_fma_f32 v[144:145], v[128:129], v[230:231], v[144:145]
	v_pk_fma_f32 v[146:147], v[118:119], v[232:233], v[146:147]
	v_pk_fma_f32 v[148:149], v[120:121], v[230:231], v[148:149]
	v_pk_fma_f32 v[150:151], v[106:107], v[232:233], v[150:151]
	v_pk_fma_f32 v[152:153], v[108:109], v[230:231], v[152:153]
	v_pk_fma_f32 v[154:155], v[94:95], v[232:233], v[154:155]
	v_pk_fma_f32 v[160:161], v[98:99], v[230:231], v[160:161]
	s_waitcnt lgkmcnt(0)
	v_pk_fma_f32 v[8:9], v[140:141], v[6:7], v[8:9]
	v_pk_fma_f32 v[144:145], v[142:143], v[4:5], v[144:145]
	v_pk_fma_f32 v[146:147], v[136:137], v[6:7], v[146:147]
	v_pk_fma_f32 v[150:151], v[122:123], v[6:7], v[150:151]
	v_pk_fma_f32 v[6:7], v[110:111], v[6:7], v[154:155]
	v_pk_mov_b32 v[154:155], v[144:145], v[8:9] op_sel:[1,0]
	v_mov_b32_e32 v145, v9
	v_pk_fma_f32 v[148:149], v[138:139], v[4:5], v[148:149]
	v_pk_add_f32 v[8:9], v[154:155], v[144:145]
	v_pk_fma_f32 v[152:153], v[124:125], v[4:5], v[152:153]
	v_pk_fma_f32 v[4:5], v[114:115], v[4:5], v[160:161]
	v_add_f32_e32 v161, v8, v9
	v_pk_mov_b32 v[8:9], v[148:149], v[146:147] op_sel:[1,0]
	v_mov_b32_e32 v149, v147
	v_pk_add_f32 v[8:9], v[8:9], v[148:149]
	s_nop 0
	v_add_f32_e32 v162, v8, v9
	v_pk_mov_b32 v[8:9], v[152:153], v[150:151] op_sel:[1,0]
	v_mov_b32_e32 v153, v151
	v_pk_add_f32 v[8:9], v[8:9], v[152:153]
	s_nop 0
	v_add_f32_e32 v130, v8, v9
	v_pk_mov_b32 v[8:9], v[4:5], v[6:7] op_sel:[1,0]
	v_mov_b32_e32 v5, v7
	v_pk_add_f32 v[4:5], v[8:9], v[4:5]
	s_nop 0
	v_add_f32_e32 v160, v4, v5
	ds_read_b128 v[230:233], v2 offset:8192
	ds_read_b128 v[4:7], v2 offset:9216
	s_waitcnt lgkmcnt(1)
	v_pk_fma_f32 v[8:9], v[26:27], v[232:233], 0 op_sel_hi:[1,1,0]
	v_pk_fma_f32 v[144:145], v[30:31], v[230:231], 0 op_sel_hi:[1,1,0]
	v_pk_fma_f32 v[146:147], v[20:21], v[232:233], 0 op_sel_hi:[1,1,0]
	v_pk_fma_f32 v[148:149], v[24:25], v[230:231], 0 op_sel_hi:[1,1,0]
	v_pk_fma_f32 v[150:151], v[14:15], v[232:233], 0 op_sel_hi:[1,1,0]
	v_pk_fma_f32 v[152:153], v[16:17], v[230:231], 0 op_sel_hi:[1,1,0]
	v_pk_fma_f32 v[154:155], v[10:11], v[232:233], 0 op_sel_hi:[1,1,0]
	v_pk_fma_f32 v[164:165], v[12:13], v[230:231], 0 op_sel_hi:[1,1,0]
	ds_read_b128 v[230:233], v2 offset:10240
	s_waitcnt lgkmcnt(1)
; __device__ __forceinline__ void ph9_router(const Frame& F, const Args& A) {
;     ...
;             for (int g = 0; g < 4; ++g) { float q[4][4];
; #pragma unroll
;                 for (int el = 0; el < 4; ++el) { f32x4 a0 = {0.f, 0.f, 0.f, 0.f}, a1 = a0, a2 = a0, a3 = a0;
; #pragma unroll
;                     for (int j = 0; j < 8; ++j) { const f32x4 w = wl[(4 * g + el) * 512 + lane + 64 * j];
;                         a0 += hv[0][j] * w; a1 += hv[1][j] * w; a2 += hv[2][j] * w; a3 += hv[3][j] * w; }
;                     q[0][el] = (a0.x + a0.y) + (a0.z + a0.w); q[1][el] = (a1.x + a1.y) + (a1.z + a1.w); q[2][el] = (a2.x + a2.y) + (a2.z + a2.w); q[3][el] = (a3.x + a3.y) + (a3.z + a3.w); }
	v_pk_fma_f32 v[8:9], v[48:49], v[6:7], v[8:9]
	v_pk_fma_f32 v[144:145], v[52:53], v[4:5], v[144:145]
	v_pk_fma_f32 v[146:147], v[38:39], v[6:7], v[146:147]
	v_pk_fma_f32 v[148:149], v[40:41], v[4:5], v[148:149]
	v_pk_fma_f32 v[150:151], v[28:29], v[6:7], v[150:151]
	v_pk_fma_f32 v[152:153], v[32:33], v[4:5], v[152:153]
	v_pk_fma_f32 v[154:155], v[18:19], v[6:7], v[154:155]
	v_pk_fma_f32 v[164:165], v[22:23], v[4:5], v[164:165]
	ds_read_b128 v[4:7], v2 offset:11264
	s_waitcnt lgkmcnt(1)
	v_pk_fma_f32 v[8:9], v[62:63], v[232:233], v[8:9]
	v_pk_fma_f32 v[144:145], v[64:65], v[230:231], v[144:145]
	v_pk_fma_f32 v[146:147], v[54:55], v[232:233], v[146:147]
	v_pk_fma_f32 v[148:149], v[56:57], v[230:231], v[148:149]
	v_pk_fma_f32 v[150:151], v[42:43], v[232:233], v[150:151]
	v_pk_fma_f32 v[152:153], v[44:45], v[230:231], v[152:153]
	v_pk_fma_f32 v[154:155], v[34:35], v[232:233], v[154:155]
	v_pk_fma_f32 v[164:165], v[36:37], v[230:231], v[164:165]
	ds_read_b128 v[230:233], v2 offset:12288
	s_waitcnt lgkmcnt(1)
	v_pk_fma_f32 v[8:9], v[76:77], v[6:7], v[8:9]
	v_pk_fma_f32 v[144:145], v[80:81], v[4:5], v[144:145]
	v_pk_fma_f32 v[146:147], v[68:69], v[6:7], v[146:147]
	v_pk_fma_f32 v[148:149], v[72:73], v[4:5], v[148:149]
	v_pk_fma_f32 v[150:151], v[58:59], v[6:7], v[150:151]
	v_pk_fma_f32 v[152:153], v[60:61], v[4:5], v[152:153]
	v_pk_fma_f32 v[154:155], v[46:47], v[6:7], v[154:155]
	v_pk_fma_f32 v[164:165], v[50:51], v[4:5], v[164:165]
	ds_read_b128 v[4:7], v2 offset:13312
	s_waitcnt lgkmcnt(1)
	v_pk_fma_f32 v[8:9], v[96:97], v[232:233], v[8:9]
	v_pk_fma_f32 v[144:145], v[100:101], v[230:231], v[144:145]
	v_pk_fma_f32 v[146:147], v[86:87], v[232:233], v[146:147]
	v_pk_fma_f32 v[148:149], v[88:89], v[230:231], v[148:149]
	v_pk_fma_f32 v[150:151], v[74:75], v[232:233], v[150:151]
	v_pk_fma_f32 v[152:153], v[78:79], v[230:231], v[152:153]
	v_pk_fma_f32 v[154:155], v[66:67], v[232:233], v[154:155]
	v_pk_fma_f32 v[164:165], v[70:71], v[230:231], v[164:165]
	ds_read_b128 v[230:233], v2 offset:14336
	s_waitcnt lgkmcnt(1)
	v_pk_fma_f32 v[8:9], v[112:113], v[6:7], v[8:9]
	v_pk_fma_f32 v[144:145], v[116:117], v[4:5], v[144:145]
	v_pk_fma_f32 v[146:147], v[102:103], v[6:7], v[146:147]
	v_pk_fma_f32 v[148:149], v[104:105], v[4:5], v[148:149]
	v_pk_fma_f32 v[150:151], v[90:91], v[6:7], v[150:151]
	v_pk_fma_f32 v[152:153], v[92:93], v[4:5], v[152:153]
	v_pk_fma_f32 v[154:155], v[82:83], v[6:7], v[154:155]
	v_pk_fma_f32 v[164:165], v[84:85], v[4:5], v[164:165]
	ds_read_b128 v[4:7], v2 offset:15360
	s_waitcnt lgkmcnt(1)
	v_pk_fma_f32 v[8:9], v[126:127], v[232:233], v[8:9]
	v_pk_fma_f32 v[144:145], v[128:129], v[230:231], v[144:145]
	v_pk_fma_f32 v[146:147], v[118:119], v[232:233], v[146:147]
	v_pk_fma_f32 v[148:149], v[120:121], v[230:231], v[148:149]
	v_pk_fma_f32 v[150:151], v[106:107], v[232:233], v[150:151]
	v_pk_fma_f32 v[152:153], v[108:109], v[230:231], v[152:153]
	v_pk_fma_f32 v[154:155], v[94:95], v[232:233], v[154:155]
	v_pk_fma_f32 v[164:165], v[98:99], v[230:231], v[164:165]
	s_waitcnt lgkmcnt(0)
	v_pk_fma_f32 v[8:9], v[140:141], v[6:7], v[8:9]
	v_pk_fma_f32 v[144:145], v[142:143], v[4:5], v[144:145]
	v_pk_fma_f32 v[146:147], v[136:137], v[6:7], v[146:147]
	v_pk_fma_f32 v[150:151], v[122:123], v[6:7], v[150:151]
	v_pk_fma_f32 v[6:7], v[110:111], v[6:7], v[154:155]
	v_pk_mov_b32 v[154:155], v[144:145], v[8:9] op_sel:[1,0]
	v_mov_b32_e32 v145, v9
	v_pk_fma_f32 v[148:149], v[138:139], v[4:5], v[148:149]
	v_pk_add_f32 v[8:9], v[154:155], v[144:145]
	v_pk_fma_f32 v[152:153], v[124:125], v[4:5], v[152:153]
	v_pk_fma_f32 v[4:5], v[114:115], v[4:5], v[164:165]
	v_add_f32_e32 v165, v8, v9
	v_pk_mov_b32 v[8:9], v[148:149], v[146:147] op_sel:[1,0]
	v_mov_b32_e32 v149, v147
	v_pk_add_f32 v[8:9], v[8:9], v[148:149]
	s_nop 0
	v_add_f32_e32 v166, v8, v9
	v_pk_mov_b32 v[8:9], v[152:153], v[150:151] op_sel:[1,0]
	v_mov_b32_e32 v153, v151
	v_pk_add_f32 v[8:9], v[8:9], v[152:153]
	s_nop 0
	v_add_f32_e32 v163, v8, v9
	v_pk_mov_b32 v[8:9], v[4:5], v[6:7] op_sel:[1,0]
	v_mov_b32_e32 v5, v7
	v_pk_add_f32 v[4:5], v[8:9], v[4:5]
	s_nop 0
	v_add_f32_e32 v164, v4, v5
	ds_read_b128 v[230:233], v2 offset:16384
	ds_read_b128 v[4:7], v2 offset:17408
	s_waitcnt lgkmcnt(1)
	v_pk_fma_f32 v[8:9], v[26:27], v[232:233], 0 op_sel_hi:[1,1,0]
	v_pk_fma_f32 v[144:145], v[30:31], v[230:231], 0 op_sel_hi:[1,1,0]
	v_pk_fma_f32 v[146:147], v[20:21], v[232:233], 0 op_sel_hi:[1,1,0]
	v_pk_fma_f32 v[148:149], v[24:25], v[230:231], 0 op_sel_hi:[1,1,0]
	v_pk_fma_f32 v[150:151], v[14:15], v[232:233], 0 op_sel_hi:[1,1,0]
	v_pk_fma_f32 v[152:153], v[16:17], v[230:231], 0 op_sel_hi:[1,1,0]
	v_pk_fma_f32 v[154:155], v[10:11], v[232:233], 0 op_sel_hi:[1,1,0]
	v_pk_fma_f32 v[174:175], v[12:13], v[230:231], 0 op_sel_hi:[1,1,0]
	ds_read_b128 v[230:233], v2 offset:18432
	s_waitcnt lgkmcnt(1)
	v_pk_fma_f32 v[8:9], v[48:49], v[6:7], v[8:9]
	v_pk_fma_f32 v[144:145], v[52:53], v[4:5], v[144:145]
	v_pk_fma_f32 v[146:147], v[38:39], v[6:7], v[146:147]
	v_pk_fma_f32 v[148:149], v[40:41], v[4:5], v[148:149]
	v_pk_fma_f32 v[150:151], v[28:29], v[6:7], v[150:151]
	v_pk_fma_f32 v[152:153], v[32:33], v[4:5], v[152:153]
	v_pk_fma_f32 v[154:155], v[18:19], v[6:7], v[154:155]
	v_pk_fma_f32 v[174:175], v[22:23], v[4:5], v[174:175]
	ds_read_b128 v[4:7], v2 offset:19456
	s_waitcnt lgkmcnt(1)
	v_pk_fma_f32 v[8:9], v[62:63], v[232:233], v[8:9]
	v_pk_fma_f32 v[144:145], v[64:65], v[230:231], v[144:145]
	v_pk_fma_f32 v[146:147], v[54:55], v[232:233], v[146:147]
	v_pk_fma_f32 v[148:149], v[56:57], v[230:231], v[148:149]
	v_pk_fma_f32 v[150:151], v[42:43], v[232:233], v[150:151]
	v_pk_fma_f32 v[152:153], v[44:45], v[230:231], v[152:153]
	v_pk_fma_f32 v[154:155], v[34:35], v[232:233], v[154:155]
	v_pk_fma_f32 v[174:175], v[36:37], v[230:231], v[174:175]
	ds_read_b128 v[230:233], v2 offset:20480
	s_waitcnt lgkmcnt(1)
; __device__ __forceinline__ void ph9_router(const Frame& F, const Args& A) {
;     ...
;             for (int g = 0; g < 4; ++g) { float q[4][4];
; #pragma unroll
;                 for (int el = 0; el < 4; ++el) { f32x4 a0 = {0.f, 0.f, 0.f, 0.f}, a1 = a0, a2 = a0, a3 = a0;
; #pragma unroll
;                     for (int j = 0; j < 8; ++j) { const f32x4 w = wl[(4 * g + el) * 512 + lane + 64 * j];
;                         a0 += hv[0][j] * w; a1 += hv[1][j] * w; a2 += hv[2][j] * w; a3 += hv[3][j] * w; }
;                     q[0][el] = (a0.x + a0.y) + (a0.z + a0.w); q[1][el] = (a1.x + a1.y) + (a1.z + a1.w); q[2][el] = (a2.x + a2.y) + (a2.z + a2.w); q[3][el] = (a3.x + a3.y) + (a3.z + a3.w); }
	v_pk_fma_f32 v[8:9], v[76:77], v[6:7], v[8:9]
	v_pk_fma_f32 v[144:145], v[80:81], v[4:5], v[144:145]
	v_pk_fma_f32 v[146:147], v[68:69], v[6:7], v[146:147]
	v_pk_fma_f32 v[148:149], v[72:73], v[4:5], v[148:149]
	v_pk_fma_f32 v[150:151], v[58:59], v[6:7], v[150:151]
	v_pk_fma_f32 v[152:153], v[60:61], v[4:5], v[152:153]
	v_pk_fma_f32 v[154:155], v[46:47], v[6:7], v[154:155]
	v_pk_fma_f32 v[174:175], v[50:51], v[4:5], v[174:175]
	ds_read_b128 v[4:7], v2 offset:21504
	s_waitcnt lgkmcnt(1)
	v_pk_fma_f32 v[8:9], v[96:97], v[232:233], v[8:9]
	v_pk_fma_f32 v[144:145], v[100:101], v[230:231], v[144:145]
	v_pk_fma_f32 v[146:147], v[86:87], v[232:233], v[146:147]
	v_pk_fma_f32 v[148:149], v[88:89], v[230:231], v[148:149]
	v_pk_fma_f32 v[150:151], v[74:75], v[232:233], v[150:151]
	v_pk_fma_f32 v[152:153], v[78:79], v[230:231], v[152:153]
	v_pk_fma_f32 v[154:155], v[66:67], v[232:233], v[154:155]
	v_pk_fma_f32 v[174:175], v[70:71], v[230:231], v[174:175]
	ds_read_b128 v[230:233], v2 offset:22528
	s_waitcnt lgkmcnt(1)
	v_pk_fma_f32 v[8:9], v[112:113], v[6:7], v[8:9]
	v_pk_fma_f32 v[144:145], v[116:117], v[4:5], v[144:145]
	v_pk_fma_f32 v[146:147], v[102:103], v[6:7], v[146:147]
	v_pk_fma_f32 v[148:149], v[104:105], v[4:5], v[148:149]
	v_pk_fma_f32 v[150:151], v[90:91], v[6:7], v[150:151]
	v_pk_fma_f32 v[152:153], v[92:93], v[4:5], v[152:153]
	v_pk_fma_f32 v[154:155], v[82:83], v[6:7], v[154:155]
	v_pk_fma_f32 v[174:175], v[84:85], v[4:5], v[174:175]
	ds_read_b128 v[4:7], v2 offset:23552
	s_waitcnt lgkmcnt(1)
	v_pk_fma_f32 v[8:9], v[126:127], v[232:233], v[8:9]
	v_pk_fma_f32 v[144:145], v[128:129], v[230:231], v[144:145]
	v_pk_fma_f32 v[146:147], v[118:119], v[232:233], v[146:147]
	v_pk_fma_f32 v[148:149], v[120:121], v[230:231], v[148:149]
	v_pk_fma_f32 v[150:151], v[106:107], v[232:233], v[150:151]
	v_pk_fma_f32 v[152:153], v[108:109], v[230:231], v[152:153]
	v_pk_fma_f32 v[154:155], v[94:95], v[232:233], v[154:155]
	v_pk_fma_f32 v[174:175], v[98:99], v[230:231], v[174:175]
	s_waitcnt lgkmcnt(0)
	v_pk_fma_f32 v[8:9], v[140:141], v[6:7], v[8:9]
	v_pk_fma_f32 v[144:145], v[142:143], v[4:5], v[144:145]
	v_pk_fma_f32 v[146:147], v[136:137], v[6:7], v[146:147]
	v_pk_fma_f32 v[150:151], v[122:123], v[6:7], v[150:151]
	v_pk_fma_f32 v[6:7], v[110:111], v[6:7], v[154:155]
	v_pk_mov_b32 v[154:155], v[144:145], v[8:9] op_sel:[1,0]
	v_mov_b32_e32 v145, v9
	v_pk_fma_f32 v[148:149], v[138:139], v[4:5], v[148:149]
	v_pk_add_f32 v[8:9], v[154:155], v[144:145]
	v_pk_fma_f32 v[152:153], v[124:125], v[4:5], v[152:153]
	v_add_f32_e32 v170, v8, v9
	v_pk_mov_b32 v[8:9], v[148:149], v[146:147] op_sel:[1,0]
	v_mov_b32_e32 v149, v147
	v_pk_add_f32 v[8:9], v[8:9], v[148:149]
	v_pk_fma_f32 v[4:5], v[114:115], v[4:5], v[174:175]
	v_add_f32_e32 v172, v8, v9
	v_pk_mov_b32 v[8:9], v[152:153], v[150:151] op_sel:[1,0]
	v_mov_b32_e32 v153, v151
	v_pk_add_f32 v[8:9], v[8:9], v[152:153]
	s_nop 0
	v_add_f32_e32 v167, v8, v9
	v_pk_mov_b32 v[8:9], v[4:5], v[6:7] op_sel:[1,0]
	v_mov_b32_e32 v5, v7
	v_pk_add_f32 v[4:5], v[8:9], v[4:5]
	s_nop 0
	v_add_f32_e32 v168, v4, v5
	ds_read_b128 v[230:233], v2 offset:24576
	ds_read_b128 v[4:7], v2 offset:25600
	s_waitcnt lgkmcnt(1)
	v_pk_fma_f32 v[8:9], v[26:27], v[232:233], 0 op_sel_hi:[1,1,0]
	v_pk_fma_f32 v[144:145], v[30:31], v[230:231], 0 op_sel_hi:[1,1,0]
	v_pk_fma_f32 v[146:147], v[20:21], v[232:233], 0 op_sel_hi:[1,1,0]
	v_pk_fma_f32 v[148:149], v[24:25], v[230:231], 0 op_sel_hi:[1,1,0]
	v_pk_fma_f32 v[150:151], v[14:15], v[232:233], 0 op_sel_hi:[1,1,0]
	v_pk_fma_f32 v[152:153], v[16:17], v[230:231], 0 op_sel_hi:[1,1,0]
	v_pk_fma_f32 v[154:155], v[10:11], v[232:233], 0 op_sel_hi:[1,1,0]
	v_pk_fma_f32 v[174:175], v[12:13], v[230:231], 0 op_sel_hi:[1,1,0]
	ds_read_b128 v[230:233], v2 offset:26624
	s_waitcnt lgkmcnt(1)
	v_pk_fma_f32 v[8:9], v[48:49], v[6:7], v[8:9]
	v_pk_fma_f32 v[144:145], v[52:53], v[4:5], v[144:145]
	v_pk_fma_f32 v[146:147], v[38:39], v[6:7], v[146:147]
	v_pk_fma_f32 v[148:149], v[40:41], v[4:5], v[148:149]
	v_pk_fma_f32 v[150:151], v[28:29], v[6:7], v[150:151]
	v_pk_fma_f32 v[152:153], v[32:33], v[4:5], v[152:153]
	v_pk_fma_f32 v[154:155], v[18:19], v[6:7], v[154:155]
	v_pk_fma_f32 v[174:175], v[22:23], v[4:5], v[174:175]
	ds_read_b128 v[4:7], v2 offset:27648
	s_waitcnt lgkmcnt(1)
	v_pk_fma_f32 v[8:9], v[62:63], v[232:233], v[8:9]
	v_pk_fma_f32 v[144:145], v[64:65], v[230:231], v[144:145]
	v_pk_fma_f32 v[146:147], v[54:55], v[232:233], v[146:147]
	v_pk_fma_f32 v[148:149], v[56:57], v[230:231], v[148:149]
	v_pk_fma_f32 v[150:151], v[42:43], v[232:233], v[150:151]
	v_pk_fma_f32 v[152:153], v[44:45], v[230:231], v[152:153]
	v_pk_fma_f32 v[154:155], v[34:35], v[232:233], v[154:155]
	v_pk_fma_f32 v[174:175], v[36:37], v[230:231], v[174:175]
	ds_read_b128 v[230:233], v2 offset:28672
	s_waitcnt lgkmcnt(1)
	v_pk_fma_f32 v[8:9], v[76:77], v[6:7], v[8:9]
	v_pk_fma_f32 v[144:145], v[80:81], v[4:5], v[144:145]
	v_pk_fma_f32 v[146:147], v[68:69], v[6:7], v[146:147]
	v_pk_fma_f32 v[148:149], v[72:73], v[4:5], v[148:149]
	v_pk_fma_f32 v[150:151], v[58:59], v[6:7], v[150:151]
	v_pk_fma_f32 v[152:153], v[60:61], v[4:5], v[152:153]
	v_pk_fma_f32 v[154:155], v[46:47], v[6:7], v[154:155]
	v_pk_fma_f32 v[174:175], v[50:51], v[4:5], v[174:175]
	s_waitcnt lgkmcnt(0)
; __device__ __forceinline__ void ph9_router(const Frame& F, const Args& A) {
;     ...
;             for (int g = 0; g < 4; ++g) { float q[4][4];
; #pragma unroll
;                 for (int el = 0; el < 4; ++el) { f32x4 a0 = {0.f, 0.f, 0.f, 0.f}, a1 = a0, a2 = a0, a3 = a0;
; #pragma unroll
;                     for (int j = 0; j < 8; ++j) { const f32x4 w = wl[(4 * g + el) * 512 + lane + 64 * j];
;                         a0 += hv[0][j] * w; a1 += hv[1][j] * w; a2 += hv[2][j] * w; a3 += hv[3][j] * w; }
;                     q[0][el] = (a0.x + a0.y) + (a0.z + a0.w); q[1][el] = (a1.x + a1.y) + (a1.z + a1.w); q[2][el] = (a2.x + a2.y) + (a2.z + a2.w); q[3][el] = (a3.x + a3.y) + (a3.z + a3.w); }
;                 float s1[2][4], s2[4], s3[2];
; #pragma unroll
;                 for (int k = 0; k < 2; ++k)
; #pragma unroll
;                     for (int el = 0; el < 4; ++el) { const float keep = b4 ? q[2 * k + 1][el] : q[2 * k][el], send = b4 ? q[2 * k][el] : q[2 * k + 1][el]; s1[k][el] = keep + __shfl_xor(send, 16); }
; #pragma unroll
;                 for (int el = 0; el < 4; ++el) { const float keep = b5 ? s1[1][el] : s1[0][el], send = b5 ? s1[0][el] : s1[1][el]; s2[el] = keep + __shfl_xor(send, 32); }
; #pragma unroll
;                 for (int k = 0; k < 2; ++k) { const float keep = b0 ? s2[2 * k + 1] : s2[2 * k], send = b0 ? s2[2 * k] : s2[2 * k + 1]; s3[k] = keep + __shfl_xor(send, 1); }
;                 float s4; { const float keep = b1 ? s3[1] : s3[0], send = b1 ? s3[0] : s3[1]; s4 = keep + __shfl_xor(send, 2); }
;                 s4 += __shfl_xor(s4, 4); s4 += __shfl_xor(s4, 8);
;                 if (((lane >> 2) & 3) == g) mine = s4; }
;             const float tot = mine + br[half * 16 + (lane & 15)];
;             if (half == 0) lgv[0] = tot; else lgv[1] = tot;
	v_pk_fma_f32 v[8:9], v[96:97], v[232:233], v[8:9]
	v_pk_fma_f32 v[144:145], v[100:101], v[230:231], v[144:145]
	v_pk_fma_f32 v[146:147], v[86:87], v[232:233], v[146:147]
	v_pk_fma_f32 v[148:149], v[88:89], v[230:231], v[148:149]
	v_pk_fma_f32 v[150:151], v[74:75], v[232:233], v[150:151]
	v_pk_fma_f32 v[152:153], v[78:79], v[230:231], v[152:153]
	v_pk_fma_f32 v[154:155], v[66:67], v[232:233], v[154:155]
	v_pk_fma_f32 v[174:175], v[70:71], v[230:231], v[174:175]
	ds_read_b128 v[4:7], v2 offset:29696
	s_waitcnt lgkmcnt(0)
	v_pk_fma_f32 v[144:145], v[116:117], v[4:5], v[144:145]
	v_pk_fma_f32 v[148:149], v[104:105], v[4:5], v[148:149]
	v_pk_fma_f32 v[152:153], v[92:93], v[4:5], v[152:153]
	v_pk_fma_f32 v[4:5], v[84:85], v[4:5], v[174:175]
	ds_read_b128 v[174:177], v2 offset:30720
	v_pk_fma_f32 v[8:9], v[112:113], v[6:7], v[8:9]
	v_pk_fma_f32 v[146:147], v[102:103], v[6:7], v[146:147]
	v_pk_fma_f32 v[150:151], v[90:91], v[6:7], v[150:151]
	v_pk_fma_f32 v[154:155], v[82:83], v[6:7], v[154:155]
	s_waitcnt lgkmcnt(0)
	v_pk_fma_f32 v[6:7], v[126:127], v[176:177], v[8:9]
	v_pk_fma_f32 v[8:9], v[128:129], v[174:175], v[144:145]
	v_pk_fma_f32 v[144:145], v[118:119], v[176:177], v[146:147]
	v_pk_fma_f32 v[146:147], v[120:121], v[174:175], v[148:149]
	v_pk_fma_f32 v[148:149], v[106:107], v[176:177], v[150:151]
	v_pk_fma_f32 v[150:151], v[108:109], v[174:175], v[152:153]
	v_pk_fma_f32 v[152:153], v[94:95], v[176:177], v[154:155]
	v_pk_fma_f32 v[154:155], v[98:99], v[174:175], v[4:5]
	ds_read_b128 v[2:5], v2 offset:31744
	s_waitcnt lgkmcnt(0)
	v_pk_fma_f32 v[6:7], v[140:141], v[4:5], v[6:7]
	v_pk_fma_f32 v[8:9], v[142:143], v[2:3], v[8:9]
	v_pk_fma_f32 v[144:145], v[136:137], v[4:5], v[144:145]
	v_pk_fma_f32 v[148:149], v[122:123], v[4:5], v[148:149]
	v_pk_fma_f32 v[4:5], v[110:111], v[4:5], v[152:153]
	v_pk_mov_b32 v[152:153], v[8:9], v[6:7] op_sel:[1,0]
	v_mov_b32_e32 v9, v7
	v_pk_fma_f32 v[146:147], v[138:139], v[2:3], v[146:147]
	v_pk_add_f32 v[6:7], v[152:153], v[8:9]
	v_pk_fma_f32 v[150:151], v[124:125], v[2:3], v[150:151]
	v_add_f32_e32 v8, v6, v7
	v_pk_mov_b32 v[6:7], v[146:147], v[144:145] op_sel:[1,0]
	v_mov_b32_e32 v147, v145
	v_pk_add_f32 v[6:7], v[6:7], v[146:147]
	v_pk_fma_f32 v[2:3], v[114:115], v[2:3], v[154:155]
	v_add_f32_e32 v9, v6, v7
	v_pk_mov_b32 v[6:7], v[150:151], v[148:149] op_sel:[1,0]
	v_mov_b32_e32 v151, v149
	v_pk_add_f32 v[6:7], v[6:7], v[150:151]
	s_nop 0
	v_add_f32_e32 v144, v6, v7
	v_pk_mov_b32 v[6:7], v[2:3], v[4:5] op_sel:[1,0]
	v_cndmask_b32_e64 v4, v161, v162, s[8:9]
	v_mov_b32_e32 v3, v5
	ds_bpermute_b32 v4, v197, v4
	v_cndmask_b32_e64 v5, v165, v166, s[8:9]
	v_pk_add_f32 v[2:3], v[6:7], v[2:3]
	ds_bpermute_b32 v5, v197, v5
	v_cndmask_b32_e64 v6, v170, v172, s[8:9]
	ds_bpermute_b32 v6, v197, v6
	v_cndmask_b32_e64 v7, v8, v9, s[8:9]
	v_add_f32_e32 v2, v2, v3
	v_cndmask_b32_e64 v3, v162, v161, s[8:9]
	ds_bpermute_b32 v7, v197, v7
	s_waitcnt lgkmcnt(3)
	v_add_f32_e32 v3, v3, v4
	v_cndmask_b32_e64 v4, v166, v165, s[8:9]
	s_waitcnt lgkmcnt(2)
	v_add_f32_e32 v4, v4, v5
	v_cndmask_b32_e64 v5, v172, v170, s[8:9]
	s_waitcnt lgkmcnt(1)
	v_add_f32_e32 v5, v5, v6
	v_cndmask_b32_e64 v6, v9, v8, s[8:9]
	v_cndmask_b32_e64 v8, v130, v160, s[8:9]
	ds_bpermute_b32 v8, v197, v8
	v_cndmask_b32_e64 v9, v163, v164, s[8:9]
	s_waitcnt lgkmcnt(1)
	v_add_f32_e32 v6, v6, v7
	v_cndmask_b32_e64 v7, v160, v130, s[8:9]
	ds_bpermute_b32 v9, v197, v9
	v_cndmask_b32_e64 v130, v167, v168, s[8:9]
	ds_bpermute_b32 v130, v197, v130
	s_waitcnt lgkmcnt(2)
	v_add_f32_e32 v7, v7, v8
	v_cndmask_b32_e64 v8, v164, v163, s[8:9]
	s_waitcnt lgkmcnt(1)
	v_add_f32_e32 v8, v8, v9
	v_cndmask_b32_e64 v9, v168, v167, s[8:9]
	s_waitcnt lgkmcnt(0)
	v_add_f32_e32 v9, v9, v130
	v_cndmask_b32_e64 v130, v2, v144, s[8:9]
	v_cndmask_b32_e64 v2, v144, v2, s[8:9]
	ds_bpermute_b32 v2, v197, v2
	s_waitcnt lgkmcnt(0)
	v_add_f32_e32 v2, v130, v2
	v_cndmask_b32_e64 v130, v7, v3, s[10:11]
	v_cndmask_b32_e64 v3, v3, v7, s[10:11]
	v_cndmask_b32_e64 v7, v8, v4, s[10:11]
	v_cndmask_b32_e64 v4, v4, v8, s[10:11]
	ds_bpermute_b32 v4, v198, v4
	ds_bpermute_b32 v3, v198, v3
	s_waitcnt lgkmcnt(1)
	v_add_f32_e32 v4, v7, v4
	v_cndmask_b32_e64 v7, v9, v5, s[10:11]
	v_cndmask_b32_e64 v5, v5, v9, s[10:11]
	ds_bpermute_b32 v5, v198, v5
	s_waitcnt lgkmcnt(1)
	v_add_f32_e32 v3, v130, v3
	s_waitcnt lgkmcnt(0)
	v_add_f32_e32 v5, v7, v5
	v_cndmask_b32_e64 v7, v2, v6, s[10:11]
	v_cndmask_b32_e64 v2, v6, v2, s[10:11]
	ds_bpermute_b32 v2, v198, v2
	v_cndmask_b32_e64 v6, v4, v3, s[4:5]
	v_cndmask_b32_e64 v3, v3, v4, s[4:5]
	ds_bpermute_b32 v3, v193, v3
	s_waitcnt lgkmcnt(1)
	v_add_f32_e32 v2, v7, v2
	v_cndmask_b32_e64 v4, v2, v5, s[4:5]
	v_cndmask_b32_e64 v2, v5, v2, s[4:5]
	ds_bpermute_b32 v2, v193, v2
	s_waitcnt lgkmcnt(1)
	v_add_f32_e32 v3, v6, v3
	s_waitcnt lgkmcnt(0)
	v_add_f32_e32 v2, v4, v2
	v_cndmask_b32_e64 v4, v2, v3, s[6:7]
	v_cndmask_b32_e64 v2, v3, v2, s[6:7]
	ds_bpermute_b32 v2, v196, v2
	s_waitcnt lgkmcnt(0)
	v_add_f32_e32 v2, v4, v2
	ds_bpermute_b32 v3, v195, v2
	s_waitcnt lgkmcnt(0)
	v_add_f32_e32 v2, v2, v3
	ds_bpermute_b32 v3, v194, v2
	s_waitcnt lgkmcnt(0)
	v_add_f32_e32 v2, v2, v3
	v_cndmask_b32_e32 v159, v159, v2, vcc
	s_cbranch_scc0 .LBB0_1199
	v_or_b32_e32 v130, s42, v156
	v_lshl_add_u64 v[2:3], v[130:131], 2, s[74:75]
	global_load_dword v2, v[2:3], off
	s_mov_b32 s42, 16
	s_and_b64 vcc, exec, s[12:13]
	s_waitcnt vmcnt(0)
	v_add_f32_e32 v2, v159, v2
	v_cndmask_b32_e64 v191, v191, v2, s[0:1]
	v_cndmask_b32_e64 v190, v2, v190, s[0:1]
	s_mov_b64 s[0:1], 0
	s_cbranch_vccnz .LBB0_1202
	s_mov_b64 s[12:13], -1
	s_branch .LBB0_1196
